# stream prologue reorder: partial-u loads and enc loads issued back to back, wait only after; on top of prep rewrite
# baseline (speedup 1.0000x reference)
_Z13stream_kernelPKfPf:
	s_load_dwordx4 s[4:7], s[0:1], 0x0
	v_readfirstlane_b32 s3, v0
	v_and_b32_e32 v24, 63, v0
	s_lshl_b32 s0, s2, 7
	v_lshlrev_b32_e32 v62, 4, v0
	v_lshlrev_b32_e32 v25, 4, v24
	s_lshr_b32 s8, s3, 6
	s_add_i32 s9, s8, s0
	s_lshl_b32 s10, s9, 12
	s_brev_b32 s2, 16
	s_mov_b32 s3, 0x20000
	v_add_u32_e32 v63, 0x1000, v62
	v_add_u32_e32 v64, 0x2000, v62
	v_add_u32_e32 v65, 0x3000, v62
	s_waitcnt lgkmcnt(0)
	s_and_b32 s1, s5, 0xffff
	s_mov_b32 s0, s4
	s_mov_b32 s4, s10
	s_add_i32 s5, s4, 0x10000
	s_add_i32 s10, s4, 0x20000
	s_cmp_lt_u32 s8, 4
	s_cbranch_scc0 .Lst_enc
	global_load_dwordx4 v[2:5], v62, s[6:7]
	global_load_dwordx4 v[6:9], v63, s[6:7]
	global_load_dwordx4 v[10:13], v64, s[6:7]
	global_load_dwordx4 v[58:61], v65, s[6:7]
.Lst_enc:
	buffer_load_dwordx4 v[26:29], v25, s[0:3], s4 offen offset:1024 nt
	buffer_load_dwordx4 v[30:33], v25, s[0:3], s4 offen nt
	buffer_load_dwordx4 v[34:37], v25, s[0:3], s4 offen offset:2048 nt
	buffer_load_dwordx4 v[38:41], v25, s[0:3], s5 offen offset:1024 nt
	buffer_load_dwordx4 v[42:45], v25, s[0:3], s5 offen nt
	buffer_load_dwordx4 v[16:19], v25, s[0:3], s4 offen offset:3072 nt
	buffer_load_dwordx4 v[46:49], v25, s[0:3], s5 offen offset:2048 nt
	buffer_load_dwordx4 v[20:23], v25, s[0:3], s5 offen offset:3072 nt
	s_cbranch_scc0 .Lst_bar
	s_waitcnt vmcnt(8)
	v_pk_add_f32 v[2:3], v[2:3], v[6:7]
	v_pk_add_f32 v[4:5], v[4:5], v[8:9]
	v_pk_add_f32 v[10:11], v[10:11], v[58:59]
	v_pk_add_f32 v[12:13], v[12:13], v[60:61]
	v_pk_add_f32 v[2:3], v[2:3], v[10:11]
	v_pk_add_f32 v[4:5], v[4:5], v[12:13]
	s_nop 0
	ds_write_b128 v62, v[2:5]
.Lst_bar:
	s_waitcnt lgkmcnt(0)
	s_barrier
	buffer_load_dwordx4 v[50:53], v25, s[0:3], s10 offen offset:1024 nt
	buffer_load_dwordx4 v[54:57], v25, s[0:3], s10 offen nt
	ds_read_b128 v[4:7], v25 offset:1024
	ds_read_b128 v[0:3], v25
	ds_read_b128 v[12:15], v25 offset:2048
	ds_read_b128 v[8:11], v25 offset:3072
	s_add_i32 s5, s4, 0x30000
	v_cmp_gt_u32_e32 vcc, 8, v24
	s_waitcnt vmcnt(9) lgkmcnt(3)
	v_pk_mul_f32 v[28:29], v[6:7], v[28:29]
	v_pk_mul_f32 v[26:27], v[4:5], v[26:27]
	s_waitcnt vmcnt(8) lgkmcnt(2)
	v_pk_fma_f32 v[32:33], v[2:3], v[32:33], v[28:29]
	v_pk_fma_f32 v[30:31], v[0:1], v[30:31], v[26:27]
	buffer_load_dwordx4 v[26:29], v25, s[0:3], s5 offen offset:1024 nt
	s_waitcnt vmcnt(8) lgkmcnt(1)
	v_pk_fma_f32 v[58:59], v[14:15], v[36:37], v[32:33]
	v_pk_fma_f32 v[60:61], v[12:13], v[34:35], v[30:31]
	buffer_load_dwordx4 v[30:33], v25, s[0:3], s5 offen nt
	s_waitcnt vmcnt(8)
	v_pk_mul_f32 v[34:35], v[6:7], v[40:41]
	v_pk_mul_f32 v[36:37], v[4:5], v[38:39]
	s_waitcnt vmcnt(7)
	v_pk_fma_f32 v[44:45], v[2:3], v[44:45], v[34:35]
	v_pk_fma_f32 v[42:43], v[0:1], v[42:43], v[36:37]
	buffer_load_dwordx4 v[34:37], v25, s[0:3], s10 offen offset:2048 nt
	s_waitcnt vmcnt(4)
	v_pk_mul_f32 v[38:39], v[6:7], v[52:53]
	v_pk_mul_f32 v[40:41], v[4:5], v[50:51]
	s_waitcnt vmcnt(3)
	v_pk_fma_f32 v[50:51], v[2:3], v[56:57], v[38:39]
	v_pk_fma_f32 v[52:53], v[0:1], v[54:55], v[40:41]
	buffer_load_dwordx4 v[38:41], v25, s[0:3], s10 offen offset:3072 nt
	v_pk_fma_f32 v[48:49], v[14:15], v[48:49], v[44:45]
	v_pk_fma_f32 v[46:47], v[12:13], v[46:47], v[42:43]
	s_waitcnt lgkmcnt(0)
	v_pk_fma_f32 v[18:19], v[10:11], v[18:19], v[58:59]
	v_pk_fma_f32 v[16:17], v[8:9], v[16:17], v[60:61]
	v_add_f32_e32 v61, v18, v19
	v_add_f32_e32 v60, v16, v17
	v_pk_fma_f32 v[16:17], v[10:11], v[22:23], v[48:49]
	v_pk_fma_f32 v[18:19], v[8:9], v[20:21], v[46:47]
	v_add_f32_e32 v16, v16, v17
	v_add_f32_e32 v18, v18, v19
	v_add_f32_e32 v60, v60, v61
	v_add_f32_e32 v16, v18, v16
	s_add_i32 s10, s4, 0x50000
	s_waitcnt vmcnt(3)
	v_pk_mul_f32 v[28:29], v[6:7], v[28:29]
	v_pk_mul_f32 v[26:27], v[4:5], v[26:27]
	v_add_f32_dpp v16, v16, v16 quad_perm:[1,0,3,2] row_mask:0xf bank_mask:0xf bound_ctrl:1
	s_waitcnt vmcnt(2)
	v_pk_fma_f32 v[54:55], v[2:3], v[32:33], v[28:29]
	v_pk_fma_f32 v[56:57], v[0:1], v[30:31], v[26:27]
	buffer_load_dwordx4 v[26:29], v25, s[0:3], s5 offen offset:2048 nt
	buffer_load_dwordx4 v[30:33], v25, s[0:3], s5 offen offset:3072 nt
	s_add_i32 s5, s4, 0x40000
	buffer_load_dwordx4 v[42:45], v25, s[0:3], s5 offen offset:1024 nt
	s_waitcnt vmcnt(4)
	v_pk_fma_f32 v[50:51], v[14:15], v[36:37], v[50:51]
	v_pk_fma_f32 v[52:53], v[12:13], v[34:35], v[52:53]
	buffer_load_dwordx4 v[34:37], v25, s[0:3], s5 offen nt
	v_add_f32_dpp v16, v16, v16 quad_perm:[2,3,0,1] row_mask:0xf bank_mask:0xf bound_ctrl:1
	s_waitcnt vmcnt(4)
	v_pk_fma_f32 v[58:59], v[10:11], v[40:41], v[50:51]
	v_pk_fma_f32 v[38:39], v[8:9], v[38:39], v[52:53]
	v_add_f32_e32 v19, v58, v59
	v_add_f32_e32 v17, v38, v39
	v_add_f32_dpp v58, v60, v60 quad_perm:[1,0,3,2] row_mask:0xf bank_mask:0xf bound_ctrl:1
	v_add_f32_e32 v18, v17, v19
	v_add_f32_dpp v16, v16, v16 row_ror:4 row_mask:0xf bank_mask:0xf bound_ctrl:1
	v_add_f32_dpp v17, v58, v58 quad_perm:[2,3,0,1] row_mask:0xf bank_mask:0xf bound_ctrl:1
	buffer_load_dwordx4 v[20:23], v25, s[0:3], s5 offen offset:2048 nt
	buffer_load_dwordx4 v[46:49], v25, s[0:3], s5 offen offset:3072 nt
	v_add_f32_dpp v17, v17, v17 row_ror:4 row_mask:0xf bank_mask:0xf bound_ctrl:1
	v_add_f32_dpp v58, v16, v16 row_ror:8 row_mask:0xf bank_mask:0xf bound_ctrl:1
	buffer_load_dwordx4 v[38:41], v25, s[0:3], s10 offen nt
	buffer_load_dwordx4 v[50:53], v25, s[0:3], s10 offen offset:1024 nt
	v_add_f32_dpp v17, v17, v17 row_ror:8 row_mask:0xf bank_mask:0xf bound_ctrl:1
	v_mov_b32_e32 v19, v17
	v_mov_b32_e32 v59, v58
	s_nop 0
	v_permlane16_swap_b32_e32 v17, v19
	v_permlane16_swap_b32_e32 v58, v59
	v_add_f32_e32 v16, v17, v19
	v_add_f32_e32 v17, v58, v59
	s_add_i32 s5, s4, 0x60000
	s_add_i32 s4, s4, 0x70000
	v_add_f32_dpp v18, v18, v18 quad_perm:[1,0,3,2] row_mask:0xf bank_mask:0xf bound_ctrl:1
	s_waitcnt vmcnt(7)
	v_pk_fma_f32 v[28:29], v[14:15], v[28:29], v[54:55]
	v_pk_fma_f32 v[54:55], v[12:13], v[26:27], v[56:57]
	s_waitcnt vmcnt(6)
	v_pk_fma_f32 v[58:59], v[10:11], v[32:33], v[28:29]
	buffer_load_dwordx4 v[26:29], v25, s[0:3], s10 offen offset:2048 nt
	v_pk_fma_f32 v[54:55], v[8:9], v[30:31], v[54:55]
	buffer_load_dwordx4 v[30:33], v25, s[0:3], s10 offen offset:3072 nt
	v_add_f32_e32 v66, v54, v55
	s_waitcnt vmcnt(7)
	v_pk_mul_f32 v[54:55], v[6:7], v[44:45]
	v_pk_mul_f32 v[56:57], v[4:5], v[42:43]
	buffer_load_dwordx4 v[42:45], v25, s[0:3], s5 offen offset:1024 nt
	s_waitcnt vmcnt(7)
	v_pk_fma_f32 v[54:55], v[2:3], v[36:37], v[54:55]
	v_pk_fma_f32 v[56:57], v[0:1], v[34:35], v[56:57]
	buffer_load_dwordx4 v[34:37], v25, s[0:3], s5 offen nt
	v_add_f32_dpp v18, v18, v18 quad_perm:[2,3,0,1] row_mask:0xf bank_mask:0xf bound_ctrl:1
	s_waitcnt vmcnt(7)
	v_pk_fma_f32 v[22:23], v[14:15], v[22:23], v[54:55]
	v_pk_fma_f32 v[20:21], v[12:13], v[20:21], v[56:57]
	s_waitcnt vmcnt(6)
	v_pk_fma_f32 v[60:61], v[10:11], v[48:49], v[22:23]
	v_pk_fma_f32 v[22:23], v[8:9], v[46:47], v[20:21]
	s_waitcnt vmcnt(4)
	v_pk_mul_f32 v[54:55], v[4:5], v[50:51]
	v_pk_mul_f32 v[20:21], v[6:7], v[52:53]
	v_pk_fma_f32 v[38:39], v[0:1], v[38:39], v[54:55]
	buffer_load_dwordx4 v[46:49], v25, s[0:3], s5 offen offset:2048 nt
	buffer_load_dwordx4 v[50:53], v25, s[0:3], s5 offen offset:3072 nt
	v_pk_fma_f32 v[20:21], v[2:3], v[40:41], v[20:21]
	v_add_f32_e32 v23, v22, v23
	v_add_f32_dpp v18, v18, v18 row_ror:4 row_mask:0xf bank_mask:0xf bound_ctrl:1
	s_waitcnt vmcnt(5)
	v_pk_fma_f32 v[26:27], v[12:13], v[26:27], v[38:39]
	buffer_load_dwordx4 v[38:41], v25, s[0:3], s4 offen nt
	buffer_load_dwordx4 v[54:57], v25, s[0:3], s4 offen offset:1024 nt
	v_pk_fma_f32 v[20:21], v[14:15], v[28:29], v[20:21]
	s_waitcnt vmcnt(6)
	v_pk_fma_f32 v[30:31], v[8:9], v[30:31], v[26:27]
	v_pk_fma_f32 v[62:63], v[10:11], v[32:33], v[20:21]
	v_add_f32_dpp v18, v18, v18 row_ror:8 row_mask:0xf bank_mask:0xf bound_ctrl:1
	s_waitcnt vmcnt(5)
	v_pk_mul_f32 v[20:21], v[6:7], v[44:45]
	v_pk_mul_f32 v[26:27], v[4:5], v[42:43]
	buffer_load_dwordx4 v[42:45], v25, s[0:3], s4 offen offset:2048 nt
	s_waitcnt vmcnt(5)
	v_pk_fma_f32 v[64:65], v[0:1], v[34:35], v[26:27]
	buffer_load_dwordx4 v[32:35], v25, s[0:3], s4 offen offset:3072 nt
	v_add_f32_e32 v27, v60, v61
	v_add_f32_e32 v23, v23, v27
	v_pk_fma_f32 v[36:37], v[2:3], v[36:37], v[20:21]
	v_add_f32_e32 v20, v58, v59
	v_add_f32_dpp v23, v23, v23 quad_perm:[1,0,3,2] row_mask:0xf bank_mask:0xf bound_ctrl:1
	v_add_f32_e32 v20, v66, v20
	v_mov_b32_e32 v19, v18
	v_add_f32_dpp v23, v23, v23 quad_perm:[2,3,0,1] row_mask:0xf bank_mask:0xf bound_ctrl:1
	v_add_f32_dpp v20, v20, v20 quad_perm:[1,0,3,2] row_mask:0xf bank_mask:0xf bound_ctrl:1
	v_permlane16_swap_b32_e32 v18, v19
	v_add_f32_dpp v23, v23, v23 row_ror:4 row_mask:0xf bank_mask:0xf bound_ctrl:1
	v_add_f32_dpp v20, v20, v20 quad_perm:[2,3,0,1] row_mask:0xf bank_mask:0xf bound_ctrl:1
	v_add_f32_e32 v18, v18, v19
	v_add_f32_dpp v23, v23, v23 row_ror:8 row_mask:0xf bank_mask:0xf bound_ctrl:1
	v_mov_b32_e32 v27, v23
	s_nop 1
	v_permlane16_swap_b32_e32 v23, v27
	v_add_f32_e32 v28, v23, v27
	v_add_f32_e32 v23, v30, v31
	s_waitcnt vmcnt(5)
	v_pk_fma_f32 v[30:31], v[14:15], v[48:49], v[36:37]
	v_pk_fma_f32 v[36:37], v[12:13], v[46:47], v[64:65]
	s_waitcnt vmcnt(4)
	v_pk_fma_f32 v[30:31], v[10:11], v[52:53], v[30:31]
	v_pk_fma_f32 v[36:37], v[8:9], v[50:51], v[36:37]
	v_add_f32_e32 v27, v62, v63
	v_add_f32_e32 v36, v36, v37
	v_add_f32_e32 v30, v30, v31
	v_add_f32_e32 v23, v23, v27
	v_add_f32_e32 v30, v36, v30
	v_add_f32_dpp v20, v20, v20 row_ror:4 row_mask:0xf bank_mask:0xf bound_ctrl:1
	v_add_f32_dpp v23, v23, v23 quad_perm:[1,0,3,2] row_mask:0xf bank_mask:0xf bound_ctrl:1
	v_add_f32_dpp v30, v30, v30 quad_perm:[1,0,3,2] row_mask:0xf bank_mask:0xf bound_ctrl:1
	v_add_f32_dpp v20, v20, v20 row_ror:8 row_mask:0xf bank_mask:0xf bound_ctrl:1
	v_add_f32_dpp v23, v23, v23 quad_perm:[2,3,0,1] row_mask:0xf bank_mask:0xf bound_ctrl:1
	v_add_f32_dpp v30, v30, v30 quad_perm:[2,3,0,1] row_mask:0xf bank_mask:0xf bound_ctrl:1
	v_mov_b32_e32 v21, v20
	v_add_f32_dpp v23, v23, v23 row_ror:4 row_mask:0xf bank_mask:0xf bound_ctrl:1
	v_add_f32_dpp v30, v30, v30 row_ror:4 row_mask:0xf bank_mask:0xf bound_ctrl:1
	v_permlane16_swap_b32_e32 v20, v21
	v_add_f32_dpp v23, v23, v23 row_ror:8 row_mask:0xf bank_mask:0xf bound_ctrl:1
	v_add_f32_dpp v30, v30, v30 row_ror:8 row_mask:0xf bank_mask:0xf bound_ctrl:1
	v_mov_b32_e32 v27, v23
	v_mov_b32_e32 v31, v30
	s_nop 0
	v_permlane16_swap_b32_e32 v23, v27
	v_permlane16_swap_b32_e32 v30, v31
	v_add_f32_e32 v21, v20, v21
	v_add_f32_e32 v23, v23, v27
	v_add_f32_e32 v30, v30, v31
	v_mov_b32_e32 v19, v16
	v_mov_b32_e32 v20, v17
	v_mov_b32_e32 v22, v18
	v_mov_b32_e32 v26, v21
	v_mov_b32_e32 v29, v28
	v_mov_b32_e32 v27, v23
	v_mov_b32_e32 v31, v30
	v_permlane32_swap_b32_e32 v16, v19
	v_permlane32_swap_b32_e32 v17, v20
	v_permlane32_swap_b32_e32 v18, v22
	v_permlane32_swap_b32_e32 v21, v26
	v_permlane32_swap_b32_e32 v28, v29
	v_permlane32_swap_b32_e32 v23, v27
	s_waitcnt vmcnt(2)
	v_pk_mul_f32 v[6:7], v[6:7], v[56:57]
	v_pk_mul_f32 v[4:5], v[4:5], v[54:55]
	v_pk_fma_f32 v[2:3], v[2:3], v[40:41], v[6:7]
	v_pk_fma_f32 v[0:1], v[0:1], v[38:39], v[4:5]
	v_permlane32_swap_b32_e32 v30, v31
	s_waitcnt vmcnt(1)
	v_pk_fma_f32 v[2:3], v[14:15], v[44:45], v[2:3]
	v_pk_fma_f32 v[0:1], v[12:13], v[42:43], v[0:1]
	s_waitcnt vmcnt(0)
	v_pk_fma_f32 v[2:3], v[10:11], v[34:35], v[2:3]
	v_pk_fma_f32 v[0:1], v[8:9], v[32:33], v[0:1]
	s_nop 0
	v_add_f32_e32 v0, v0, v1
	v_add_f32_e32 v1, v2, v3
	v_add_f32_e32 v0, v0, v1
	s_nop 1
	v_add_f32_dpp v0, v0, v0 quad_perm:[1,0,3,2] row_mask:0xf bank_mask:0xf bound_ctrl:1
	s_nop 1
	v_add_f32_dpp v0, v0, v0 quad_perm:[2,3,0,1] row_mask:0xf bank_mask:0xf bound_ctrl:1
	s_nop 1
	v_add_f32_dpp v0, v0, v0 row_ror:4 row_mask:0xf bank_mask:0xf bound_ctrl:1
	s_nop 1
	v_add_f32_dpp v0, v0, v0 row_ror:8 row_mask:0xf bank_mask:0xf bound_ctrl:1
	v_mov_b32_e32 v1, v0
	s_nop 1
	v_permlane16_swap_b32_e32 v0, v1
	v_add_f32_e32 v0, v0, v1
	v_mov_b32_e32 v1, v0
	s_nop 1
	v_permlane32_swap_b32_e32 v0, v1
	s_and_saveexec_b64 s[0:1], vcc
	s_cbranch_execz .LBB1_4
	v_add_f32_e32 v6, v16, v19
	v_cmp_eq_u32_e32 vcc, 0, v24
	v_add_f32_e32 v5, v17, v20
	v_add_f32_e32 v4, v18, v22
	v_cndmask_b32_e32 v6, 0, v6, vcc
	v_cmp_eq_u32_e32 vcc, 1, v24
	v_add_f32_e32 v3, v21, v26
	v_add_f32_e32 v2, v28, v29
	v_cndmask_b32_e32 v5, v6, v5, vcc
	v_cmp_eq_u32_e32 vcc, 2, v24
	v_add_f32_e32 v0, v0, v1
	v_add_f32_e32 v1, v30, v31
	v_cndmask_b32_e32 v4, v5, v4, vcc
	v_cmp_eq_u32_e32 vcc, 3, v24
	s_lshl_b32 s0, s8, 13
	s_and_b32 s0, s0, 0x1e000
	v_cndmask_b32_e32 v3, v4, v3, vcc
	v_cmp_eq_u32_e32 vcc, 4, v24
	s_add_u32 s0, s6, s0
	s_addc_u32 s1, s7, 0
	v_cndmask_b32_e32 v2, v3, v2, vcc
	v_add_f32_e32 v3, v23, v27
	v_cmp_eq_u32_e32 vcc, 5, v24
	s_nop 1
	v_cndmask_b32_e32 v2, v2, v3, vcc
	v_cmp_eq_u32_e32 vcc, 6, v24
	s_nop 1
	v_cndmask_b32_e32 v1, v2, v1, vcc
	v_cmp_eq_u32_e32 vcc, 7, v24
	s_nop 1
	v_cndmask_b32_e32 v2, v1, v0, vcc
	v_add_u32_e32 v0, s9, v25
	v_ashrrev_i32_e32 v0, 4, v0
	v_ashrrev_i32_e32 v1, 31, v0
	v_lshl_add_u64 v[0:1], v[0:1], 2, s[0:1]
	v_add_co_u32_e32 v0, vcc, 0x6000, v0
	s_nop 1
	v_addc_co_u32_e32 v1, vcc, 0, v1, vcc
	global_store_dword v[0:1], v2, off offset:64
